# baseline (speedup 1.0000x reference)
_Z11gemm_kernelPKfPKDF16bS0_Pf:
	s_lshr_b32 s27, s2, 3
	s_and_b32 s27, s27, 3
	s_cmp_eq_u32 s27, 0
	s_cbranch_scc1 .Lskew_done
.Lskew:
	s_sleep 8
	s_sub_u32 s27, s27, 1
	s_cmp_lg_u32 s27, 0
	s_cbranch_scc1 .Lskew
.Lskew_done:
	s_and_b32 s3, s2, 7
	s_ashr_i32 s14, s2, 3
	s_lshl_b32 s12, s3, 6
	s_load_dwordx8 s[4:11], s[0:1], 0x0
	s_add_i32 s12, s12, s14
	s_bfe_u32 s18, s2, 0x10002
	s_lshl_b32 s2, s12, 6
	s_lshl_b32 s13, s18, 14
	s_and_b32 s2, s2, 0x3f00
	v_lshrrev_b32_e32 v52, 6, v0
	v_and_b32_e32 v50, 15, v0
	v_bfe_u32 v51, v0, 4, 2
	v_bfe_u32 v1, v0, 3, 3
	s_or_b32 s2, s2, s13
	v_lshl_or_b32 v102, v52, 2, v51
	v_lshl_or_b32 v104, v52, 3, v1
	v_lshlrev_b32_e32 v1, 4, v50
	s_lshl_b32 s15, s2, 9
	s_waitcnt lgkmcnt(0)
	v_and_b32_e32 v238, 3, v52
	v_lshlrev_b32_e32 v238, 6, v238
	v_lshl_or_b32 v238, v51, 2, v238
	v_lshlrev_b32_e32 v238, 2, v238
	s_and_b32 s24, s12, 3
	s_lshl_b32 s24, s24, 8
	s_lshl_b32 s25, s18, 10
	s_add_u32 s24, s24, s25
	s_lshl_b32 s24, s24, 2
	s_add_u32 s24, s8, s24
	s_addc_u32 s25, s9, 0
	global_load_dwordx4 v[240:243], v238, s[24:25]
	global_load_dwordx4 v[244:247], v238, s[24:25] offset:64
	global_load_dwordx4 v[248:251], v238, s[24:25] offset:128
	global_load_dwordx4 v[252:255], v238, s[24:25] offset:192
	s_mov_b64 s[0:1], s[6:7]
	s_and_b32 s5, s5, 0xffff
	s_mov_b32 s7, 0x20000
	s_brev_b32 s6, -2
	v_lshl_or_b32 v1, v102, 9, v1
	s_or_b32 s2, s15, 0x4000
	s_lshl_b32 s14, s14, 8
	v_lshlrev_b32_e32 v103, 3, v0
	buffer_load_dwordx4 v[54:57], v1, s[4:7], s15 offen sc0 nt
	buffer_load_dwordx4 v[58:61], v1, s[4:7], s2 offen sc0 nt
	s_or_b32 s2, s15, 0x8000
	s_or_b32 s3, s15, 0xc000
	s_lshl_b32 s19, s18, 10
	s_and_b32 s20, s14, 0x300
	v_and_b32_e32 v105, 56, v103
	buffer_load_dwordx4 v[62:65], v1, s[4:7], s2 offen sc0 nt
	buffer_load_dwordx4 v[66:69], v1, s[4:7], s3 offen sc0 nt
	s_or_b32 s2, s15, 0x10000
	s_or_b32 s3, s15, 0x14000
	s_or_b32 s14, s19, s20
	v_lshlrev_b32_e32 v106, 1, v105
	buffer_load_dwordx4 v[70:73], v1, s[4:7], s2 offen sc0 nt
	buffer_load_dwordx4 v[74:77], v1, s[4:7], s3 offen sc0 nt
	s_or_b32 s2, s15, 0x18000
	s_or_b32 s3, s15, 0x1c000
	s_lshl_b32 s14, s14, 11
	buffer_load_dwordx4 v[78:81], v1, s[4:7], s2 offen sc0 nt
	buffer_load_dwordx4 v[82:85], v1, s[4:7], s3 offen sc0 nt
	s_and_b32 s1, s1, 0xffff
	s_mov_b32 s2, s6
	s_mov_b32 s3, s7
	v_lshl_or_b32 v188, v104, 7, v106
	s_or_b32 s16, s14, 0x2000
	buffer_load_dwordx4 v[86:89], v188, s[0:3], s14 offen sc1
	buffer_load_dwordx4 v[90:93], v188, s[0:3], s16 offen sc1
	s_or_b32 s16, s14, 0x4000
	s_or_b32 s17, s14, 0x6000
	buffer_load_dwordx4 v[94:97], v188, s[0:3], s16 offen sc1
	buffer_load_dwordx4 v[98:101], v188, s[0:3], s17 offen sc1
	s_or_b32 s16, s15, 0x100
	s_or_b32 s17, s15, 0x4100
	buffer_load_dwordx4 v[10:13], v1, s[4:7], s16 offen sc0 nt
	buffer_load_dwordx4 v[18:21], v1, s[4:7], s17 offen sc0 nt
	s_or_b32 s16, s15, 0x8100
	s_or_b32 s17, s15, 0xc100
	buffer_load_dwordx4 v[22:25], v1, s[4:7], s16 offen sc0 nt
	buffer_load_dwordx4 v[30:33], v1, s[4:7], s17 offen sc0 nt
	s_or_b32 s16, s15, 0x10100
	s_or_b32 s17, s15, 0x14100
	buffer_load_dwordx4 v[34:37], v1, s[4:7], s16 offen sc0 nt
	buffer_load_dwordx4 v[38:41], v1, s[4:7], s17 offen sc0 nt
	s_or_b32 s16, s15, 0x18100
	s_or_b32 s15, s15, 0x1c100
	buffer_load_dwordx4 v[42:45], v1, s[4:7], s16 offen sc0 nt
	buffer_load_dwordx4 v[46:49], v1, s[4:7], s15 offen sc0 nt
	s_or_b32 s15, s14, 0x8000
	s_or_b32 s16, s14, 0xa000
	buffer_load_dwordx4 v[2:5], v188, s[0:3], s15 offen sc1
	buffer_load_dwordx4 v[6:9], v188, s[0:3], s16 offen sc1
	s_or_b32 s15, s14, 0xc000
	s_or_b32 s16, s14, 0xe000
	buffer_load_dwordx4 v[14:17], v188, s[0:3], s15 offen sc1
	buffer_load_dwordx4 v[26:29], v188, s[0:3], s16 offen sc1
	v_lshrrev_b32_e32 v107, 7, v0
	v_bfe_u32 v108, v0, 3, 1
	v_lshlrev_b32_e32 v102, 6, v102
	s_movk_i32 s2, 0x3c0
	v_and_or_b32 v102, v102, s2, v105
	v_lshrrev_b32_e32 v105, 2, v0
	v_and_or_b32 v107, v107, 2, v108
	v_and_b32_e32 v105, 32, v105
	v_lshlrev_b32_e32 v107, 10, v107
	v_bfe_u32 v103, v103, 5, 1
	v_lshlrev_b32_e32 v104, 6, v104
	v_and_b32_e32 v106, 48, v106
	v_bitop3_b32 v189, v102, v107, v105 bitop3:0xde
	v_and_or_b32 v103, v52, 6, v103
	v_and_or_b32 v104, v104, s2, v106
	v_lshrrev_b32_e32 v106, 1, v0
	v_lshlrev_b32_e32 v103, 10, v103
	v_and_b32_e32 v106, 32, v106
	v_bitop3_b32 v190, v104, v103, v106 bitop3:0xde
	v_lshrrev_b32_e32 v53, 8, v0
	s_movk_i32 s15, 0x4000
	s_mov_b32 s16, 0x8000
	s_mov_b32 s17, 0xc000
	s_waitcnt vmcnt(23)
	v_cvt_pk_bf16_f32 v57, v56, v57
	v_cvt_pk_bf16_f32 v56, v54, v55
	s_waitcnt vmcnt(22)
	v_cvt_pk_bf16_f32 v55, v60, v61
	v_cvt_pk_bf16_f32 v54, v58, v59
	ds_write2st64_b64 v189, v[56:57], v[54:55] offset1:8
	s_waitcnt vmcnt(21)
	v_cvt_pk_bf16_f32 v55, v64, v65
	v_cvt_pk_bf16_f32 v54, v62, v63
	s_waitcnt vmcnt(20)
	v_cvt_pk_bf16_f32 v57, v68, v69
	v_cvt_pk_bf16_f32 v56, v66, v67
	ds_write2st64_b64 v189, v[54:55], v[56:57] offset0:16 offset1:24
	s_waitcnt vmcnt(19)
	v_cvt_pk_bf16_f32 v55, v72, v73
	v_cvt_pk_bf16_f32 v54, v70, v71
	s_waitcnt vmcnt(18)
	v_cvt_pk_bf16_f32 v57, v76, v77
	v_cvt_pk_bf16_f32 v56, v74, v75
	ds_write2st64_b64 v189, v[54:55], v[56:57] offset0:32 offset1:40
	s_waitcnt vmcnt(17)
	v_cvt_pk_bf16_f32 v55, v80, v81
	v_cvt_pk_bf16_f32 v54, v78, v79
	s_waitcnt vmcnt(16)
	v_cvt_pk_bf16_f32 v57, v84, v85
	v_cvt_pk_bf16_f32 v56, v82, v83
	ds_write2st64_b64 v189, v[54:55], v[56:57] offset0:48 offset1:56
	s_waitcnt vmcnt(15)
	ds_write_b128 v190, v[86:89] offset:32768
	s_waitcnt vmcnt(14)
	ds_write_b128 v190, v[90:93] offset:40960
	s_waitcnt vmcnt(13)
	ds_write_b128 v190, v[94:97] offset:49152
	s_waitcnt vmcnt(12)
	ds_write_b128 v190, v[98:101] offset:57344
	s_waitcnt lgkmcnt(0)
	s_barrier
	v_cmp_eq_u32_e32 vcc, 1, v53
	s_and_saveexec_b64 s[2:3], vcc
	s_cbranch_execz .LBB1_2
	s_barrier
